# indexer pass A stores group scores to dead d_ws scratch; pass B reads them back for t<248 instead of recomputing (bit-identical scores)
# speedup vs baseline: 1.0301x; 1.0059x over previous
.LBB0_1297:
	v_readlane_b32 s14, v254, 48
	v_readlane_b32 s15, v254, 49
	s_andn2_b64 vcc, exec, s[14:15]
	s_cbranch_vccnz .LBB0_1558
	s_waitcnt lgkmcnt(0)
	s_add_u32 s22, s20, 0x2c200000
	s_addc_u32 s23, s21, 0
	s_add_u32 s18, s20, 0x3f700000
	s_addc_u32 s19, s21, 0
	s_add_u32 s24, s20, 0x2c400000
	s_addc_u32 s25, s21, 0
	s_add_u32 s26, s20, 0x2b200000
	v_readlane_b32 s14, v255, 0
	s_addc_u32 s27, s21, 0
	s_mov_b32 s76, s14
	s_lshl_b32 s100, s14, 19
	s_add_u32 s100, s100, 0x35d00000
	s_add_u32 s100, s20, s100
	s_addc_u32 s101, s21, 0
	v_mbcnt_lo_u32_b32 v230, -1, 0
	v_mbcnt_hi_u32_b32 v230, -1, v230
	v_lshlrev_b32_e32 v230, 5, v230
	v_readlane_b32 s15, v255, 1
	s_branch .LBB0_1300

.LBB0_1308:
	s_waitcnt vmcnt(5)
	v_mfma_f32_16x16x32_bf16 v[130:133], v[116:119], v[0:3], 0
	s_min_i32 s32, s15, 0xf8
	v_lshl_add_u32 v231, s32, 11, v230
	s_add_i32 s31, s15, 8
	s_min_i32 s35, s31, s14
	v_lshl_or_b32 v72, s35, 5, v125
	s_waitcnt vmcnt(3)
	v_mfma_f32_16x16x32_bf16 v[134:137], v[112:115], v[0:3], 0
	v_ashrrev_i32_e32 v73, 31, v72
	v_lshlrev_b64 v[72:73], 7, v[72:73]
	v_sub_u32_e32 v72, v72, v229
	v_lshl_add_u64 v[84:85], v[120:121], 0, v[72:73]
	v_mfma_f32_16x16x32_bf16 v[138:141], v[108:111], v[4:7], v[130:133]
	global_load_dwordx4 v[72:75], v[84:85], off
	global_load_dwordx4 v[76:79], v[84:85], off offset:1024
	global_load_dwordx4 v[80:83], v[84:85], off offset:2048
	s_nop 0
	global_load_dwordx4 v[84:87], v[84:85], off offset:3072
	v_mov_b32_e32 v156, 0
	s_add_i32 s15, s15, 16
	s_waitcnt vmcnt(6)
	v_mfma_f32_16x16x32_bf16 v[132:135], v[104:107], v[4:7], v[134:137]
	v_max_i32_e32 v123, 0, v138
	v_fmac_f32_e32 v156, v12, v123
	v_mov_b32_e32 v160, 0
	s_min_i32 s35, s15, s14
	s_cmp_ge_i32 s31, s82
	s_nop 3
	v_max_i32_e32 v124, 0, v132
	v_fmac_f32_e32 v160, v12, v124
	v_max_i32_e32 v124, 0, v139
	v_mov_b32_e32 v157, 0
	v_fmac_f32_e32 v157, v12, v124
	v_max_i32_e32 v129, 0, v133
	v_mov_b32_e32 v161, 0
	v_fmac_f32_e32 v161, v12, v129
	v_max_i32_e32 v129, 0, v140
	v_mov_b32_e32 v158, 0
	v_fmac_f32_e32 v158, v12, v129
	v_max_i32_e32 v130, 0, v134
	v_mov_b32_e32 v162, 0
	v_mfma_f32_16x16x32_bf16 v[136:139], v[116:119], v[16:19], 0
	v_fmac_f32_e32 v162, v12, v130
	v_max_i32_e32 v130, 0, v141
	v_mov_b32_e32 v159, 0
	v_mfma_f32_16x16x32_bf16 v[140:143], v[112:115], v[16:19], 0
	v_fmac_f32_e32 v159, v12, v130
	v_max_i32_e32 v135, 0, v135
	v_mov_b32_e32 v163, 0
	v_mfma_f32_16x16x32_bf16 v[136:139], v[108:111], v[20:23], v[136:139]
	v_fmac_f32_e32 v163, v12, v135
	v_mfma_f32_16x16x32_bf16 v[140:143], v[104:107], v[20:23], v[140:143]
	s_nop 6
	v_max_i32_e32 v135, 0, v136
	v_fmac_f32_e32 v156, v13, v135
	v_max_i32_e32 v135, 0, v140
	v_fmac_f32_e32 v160, v13, v135
	v_max_i32_e32 v135, 0, v137
	v_fmac_f32_e32 v157, v13, v135
	v_max_i32_e32 v135, 0, v141
	v_fmac_f32_e32 v161, v13, v135
	v_max_i32_e32 v135, 0, v138
	v_fmac_f32_e32 v158, v13, v135
	v_max_i32_e32 v135, 0, v142
	v_fmac_f32_e32 v162, v13, v135
	v_max_i32_e32 v135, 0, v139
	v_mfma_f32_16x16x32_bf16 v[136:139], v[116:119], v[24:27], 0
	v_fmac_f32_e32 v159, v13, v135
	v_max_i32_e32 v135, 0, v143
	v_fmac_f32_e32 v163, v13, v135
	v_mfma_f32_16x16x32_bf16 v[140:143], v[112:115], v[24:27], 0
	v_mfma_f32_16x16x32_bf16 v[136:139], v[108:111], v[28:31], v[136:139]
	v_mfma_f32_16x16x32_bf16 v[140:143], v[104:107], v[28:31], v[140:143]
	s_nop 6
	v_max_i32_e32 v135, 0, v136
	v_fmac_f32_e32 v156, v14, v135
	v_max_i32_e32 v135, 0, v140
	v_fmac_f32_e32 v160, v14, v135
	v_max_i32_e32 v135, 0, v137
	v_fmac_f32_e32 v157, v14, v135
	v_max_i32_e32 v135, 0, v141
	v_fmac_f32_e32 v161, v14, v135
	v_max_i32_e32 v135, 0, v138
	v_fmac_f32_e32 v158, v14, v135
	v_max_i32_e32 v135, 0, v142
	v_fmac_f32_e32 v162, v14, v135
	v_max_i32_e32 v135, 0, v139
	v_mfma_f32_16x16x32_bf16 v[136:139], v[116:119], v[32:35], 0
	v_fmac_f32_e32 v159, v14, v135
	v_max_i32_e32 v135, 0, v143
	v_fmac_f32_e32 v163, v14, v135
	v_mfma_f32_16x16x32_bf16 v[140:143], v[112:115], v[32:35], 0
	v_mfma_f32_16x16x32_bf16 v[136:139], v[108:111], v[36:39], v[136:139]
	v_mfma_f32_16x16x32_bf16 v[140:143], v[104:107], v[36:39], v[140:143]
	s_nop 6
	v_max_i32_e32 v135, 0, v136
	v_fmac_f32_e32 v156, v15, v135
	v_max_i32_e32 v135, 0, v140
	v_fmac_f32_e32 v160, v15, v135
	v_max_i32_e32 v135, 0, v137
	v_fmac_f32_e32 v157, v15, v135
	v_max_i32_e32 v135, 0, v141
	v_fmac_f32_e32 v161, v15, v135
	v_max_i32_e32 v135, 0, v138
	v_fmac_f32_e32 v158, v15, v135
	v_max_i32_e32 v135, 0, v142
	v_fmac_f32_e32 v162, v15, v135
	v_max_i32_e32 v135, 0, v139
	v_mfma_f32_16x16x32_bf16 v[136:139], v[116:119], v[40:43], 0
	v_fmac_f32_e32 v159, v15, v135
	v_max_i32_e32 v135, 0, v143
	v_fmac_f32_e32 v163, v15, v135
	v_mfma_f32_16x16x32_bf16 v[140:143], v[112:115], v[40:43], 0
	v_mfma_f32_16x16x32_bf16 v[136:139], v[108:111], v[44:47], v[136:139]
	v_mfma_f32_16x16x32_bf16 v[140:143], v[104:107], v[44:47], v[140:143]
	s_nop 6
	v_max_i32_e32 v135, 0, v136
	v_fmac_f32_e32 v156, v8, v135
	v_max_i32_e32 v135, 0, v140
	v_fmac_f32_e32 v160, v8, v135
	v_max_i32_e32 v135, 0, v137
	v_fmac_f32_e32 v157, v8, v135
	v_max_i32_e32 v135, 0, v141
	v_fmac_f32_e32 v161, v8, v135
	v_max_i32_e32 v135, 0, v138
	v_fmac_f32_e32 v158, v8, v135
	v_max_i32_e32 v135, 0, v142
	v_fmac_f32_e32 v162, v8, v135
	v_max_i32_e32 v135, 0, v139
	v_mfma_f32_16x16x32_bf16 v[136:139], v[116:119], v[48:51], 0
	v_fmac_f32_e32 v159, v8, v135
	v_max_i32_e32 v135, 0, v143
	v_fmac_f32_e32 v163, v8, v135
	v_mfma_f32_16x16x32_bf16 v[140:143], v[112:115], v[48:51], 0
	v_mfma_f32_16x16x32_bf16 v[136:139], v[108:111], v[52:55], v[136:139]
	v_mfma_f32_16x16x32_bf16 v[140:143], v[104:107], v[52:55], v[140:143]
	s_nop 6
	v_max_i32_e32 v135, 0, v136
	v_fmac_f32_e32 v156, v9, v135
	v_max_i32_e32 v135, 0, v140
	v_fmac_f32_e32 v160, v9, v135
	v_max_i32_e32 v135, 0, v137
	v_fmac_f32_e32 v157, v9, v135
	v_max_i32_e32 v135, 0, v141
	v_fmac_f32_e32 v161, v9, v135
	v_max_i32_e32 v135, 0, v138
	v_fmac_f32_e32 v158, v9, v135
	v_max_i32_e32 v135, 0, v142
	v_fmac_f32_e32 v162, v9, v135
	v_max_i32_e32 v135, 0, v139
	v_mfma_f32_16x16x32_bf16 v[136:139], v[116:119], v[56:59], 0
	v_fmac_f32_e32 v159, v9, v135
	v_max_i32_e32 v135, 0, v143
	v_fmac_f32_e32 v163, v9, v135
	v_mfma_f32_16x16x32_bf16 v[140:143], v[112:115], v[56:59], 0
	v_mfma_f32_16x16x32_bf16 v[112:115], v[112:115], v[64:67], 0
	v_mfma_f32_16x16x32_bf16 v[116:119], v[116:119], v[64:67], 0
	v_mfma_f32_16x16x32_bf16 v[136:139], v[108:111], v[60:63], v[136:139]
	v_mfma_f32_16x16x32_bf16 v[140:143], v[104:107], v[60:63], v[140:143]
	v_mfma_f32_16x16x32_bf16 v[104:107], v[104:107], v[68:71], v[112:115]
	s_nop 5
	v_max_i32_e32 v135, 0, v136
	v_fmac_f32_e32 v156, v10, v135
	v_max_i32_e32 v135, 0, v140
	v_mfma_f32_16x16x32_bf16 v[108:111], v[108:111], v[68:71], v[116:119]
	v_fmac_f32_e32 v160, v10, v135
	v_max_i32_e32 v104, 0, v104
	v_max_i32_e32 v135, 0, v137
	v_fmac_f32_e32 v157, v10, v135
	v_fmac_f32_e32 v160, v11, v104
	s_nop 5
	v_max_i32_e32 v104, 0, v109
	v_max_i32_e32 v135, 0, v141
	v_fmac_f32_e32 v161, v10, v135
	v_fmac_f32_e32 v157, v11, v104
	v_max_i32_e32 v104, 0, v105
	v_max_i32_e32 v135, 0, v138
	v_fmac_f32_e32 v158, v10, v135
	v_fmac_f32_e32 v161, v11, v104
	v_max_i32_e32 v104, 0, v110
	v_max_i32_e32 v135, 0, v142
	v_fmac_f32_e32 v162, v10, v135
	v_fmac_f32_e32 v158, v11, v104
	v_max_i32_e32 v104, 0, v106
	v_max_i32_e32 v135, 0, v139
	v_fmac_f32_e32 v159, v10, v135
	v_fmac_f32_e32 v162, v11, v104
	v_max_i32_e32 v104, 0, v111
	v_max_i32_e32 v135, 0, v143
	v_fmac_f32_e32 v163, v10, v135
	v_fmac_f32_e32 v159, v11, v104
	v_max_i32_e32 v104, 0, v107
	v_max_i32_e32 v108, 0, v108
	v_fmac_f32_e32 v156, v11, v108
	v_fmac_f32_e32 v163, v11, v104
	s_nop 0
	global_store_dwordx4 v231, v[156:159], s[100:101]
	global_store_dwordx4 v231, v[160:163], s[100:101] offset:16
	v_lshrrev_b32 v104, 22, v156
	v_bfe_u32 v105, v156, 21, 1
	v_lshl_add_u32 v104, v104, 2, v128
	v_mad_u32_u24 v105, v105, s1, 1
	ds_add_u32 v104, v105
	v_lshrrev_b32 v104, 22, v157
	v_bfe_u32 v105, v157, 21, 1
	v_lshl_add_u32 v104, v104, 2, v128
	v_mad_u32_u24 v105, v105, s1, 1
	ds_add_u32 v104, v105
	v_lshrrev_b32 v104, 22, v158
	v_bfe_u32 v105, v158, 21, 1
	v_lshl_add_u32 v104, v104, 2, v128
	v_mad_u32_u24 v105, v105, s1, 1
	ds_add_u32 v104, v105
	v_lshrrev_b32 v104, 22, v159
	v_bfe_u32 v105, v159, 21, 1
	v_lshl_add_u32 v104, v104, 2, v128
	v_mad_u32_u24 v105, v105, s1, 1
	ds_add_u32 v104, v105
	v_lshrrev_b32 v104, 22, v160
	v_bfe_u32 v105, v160, 21, 1
	v_lshl_add_u32 v104, v104, 2, v128
	v_mad_u32_u24 v105, v105, s1, 1
	ds_add_u32 v104, v105
	v_lshrrev_b32 v104, 22, v161
	v_bfe_u32 v105, v161, 21, 1
	v_lshl_add_u32 v104, v104, 2, v128
	v_mad_u32_u24 v105, v105, s1, 1
	ds_add_u32 v104, v105
	v_lshrrev_b32 v104, 22, v162
	v_bfe_u32 v105, v162, 21, 1
	v_lshl_add_u32 v104, v104, 2, v128
	v_mad_u32_u24 v105, v105, s1, 1
	ds_add_u32 v104, v105
	v_lshrrev_b32 v104, 22, v163
	v_bfe_u32 v105, v163, 21, 1
	v_lshl_add_u32 v104, v104, 2, v128
	v_mad_u32_u24 v105, v105, s1, 1
	ds_add_u32 v104, v105
	v_lshl_or_b32 v104, s35, 5, v125
	v_ashrrev_i32_e32 v105, 31, v104
	v_lshlrev_b64 v[104:105], 7, v[104:105]
	v_sub_u32_e32 v104, v104, v229
	v_lshl_add_u64 v[104:105], v[120:121], 0, v[104:105]
	global_load_dwordx4 v[116:119], v[104:105], off
	global_load_dwordx4 v[108:111], v[104:105], off offset:1024
	global_load_dwordx4 v[112:115], v[104:105], off offset:2048
	s_nop 0
	global_load_dwordx4 v[104:107], v[104:105], off offset:3072
	s_cbranch_scc1 .LBB0_1307
	s_waitcnt vmcnt(9)
	v_mfma_f32_16x16x32_bf16 v[130:133], v[72:75], v[0:3], 0
	s_min_i32 s32, s31, 0xf8
	v_lshl_add_u32 v232, s32, 11, v230
	s_waitcnt vmcnt(7)
	v_mfma_f32_16x16x32_bf16 v[134:137], v[80:83], v[0:3], 0
	v_mfma_f32_16x16x32_bf16 v[138:141], v[76:79], v[4:7], v[130:133]
	s_waitcnt vmcnt(6)
	v_mfma_f32_16x16x32_bf16 v[132:135], v[84:87], v[4:7], v[134:137]
	s_nop 2
	v_mov_b32_e32 v156, 0
	s_nop 1
	v_max_i32_e32 v123, 0, v138
	v_fmac_f32_e32 v156, v12, v123
	v_mov_b32_e32 v160, 0
	v_max_i32_e32 v124, 0, v132
	v_fmac_f32_e32 v160, v12, v124
	v_max_i32_e32 v124, 0, v139
	v_mov_b32_e32 v157, 0
	v_fmac_f32_e32 v157, v12, v124
	v_max_i32_e32 v129, 0, v133
	v_mov_b32_e32 v161, 0
	v_fmac_f32_e32 v161, v12, v129
	v_max_i32_e32 v129, 0, v140
	v_mov_b32_e32 v158, 0
	v_fmac_f32_e32 v158, v12, v129
	v_max_i32_e32 v130, 0, v134
	v_mov_b32_e32 v162, 0
	v_mfma_f32_16x16x32_bf16 v[136:139], v[72:75], v[16:19], 0
	v_fmac_f32_e32 v162, v12, v130
	v_max_i32_e32 v130, 0, v141
	v_mov_b32_e32 v159, 0
	v_mfma_f32_16x16x32_bf16 v[140:143], v[80:83], v[16:19], 0
	v_fmac_f32_e32 v159, v12, v130
	v_max_i32_e32 v135, 0, v135
	v_mov_b32_e32 v163, 0
	v_mfma_f32_16x16x32_bf16 v[136:139], v[76:79], v[20:23], v[136:139]
	v_fmac_f32_e32 v163, v12, v135
	v_mfma_f32_16x16x32_bf16 v[140:143], v[84:87], v[20:23], v[140:143]
	s_nop 6
	v_max_i32_e32 v135, 0, v136
	v_fmac_f32_e32 v156, v13, v135
	v_max_i32_e32 v135, 0, v140
	v_fmac_f32_e32 v160, v13, v135
	v_max_i32_e32 v135, 0, v137
	v_fmac_f32_e32 v157, v13, v135
	v_max_i32_e32 v135, 0, v141
	v_fmac_f32_e32 v161, v13, v135
	v_max_i32_e32 v135, 0, v138
	v_fmac_f32_e32 v158, v13, v135
	v_max_i32_e32 v135, 0, v142
	v_fmac_f32_e32 v162, v13, v135
	v_max_i32_e32 v135, 0, v139
	v_mfma_f32_16x16x32_bf16 v[136:139], v[72:75], v[24:27], 0
	v_fmac_f32_e32 v159, v13, v135
	v_max_i32_e32 v135, 0, v143
	v_fmac_f32_e32 v163, v13, v135
	v_mfma_f32_16x16x32_bf16 v[140:143], v[80:83], v[24:27], 0
	v_mfma_f32_16x16x32_bf16 v[136:139], v[76:79], v[28:31], v[136:139]
	v_mfma_f32_16x16x32_bf16 v[140:143], v[84:87], v[28:31], v[140:143]
	s_nop 6
	v_max_i32_e32 v135, 0, v136
	v_fmac_f32_e32 v156, v14, v135
	v_max_i32_e32 v135, 0, v140
	v_fmac_f32_e32 v160, v14, v135
	v_max_i32_e32 v135, 0, v137
	v_fmac_f32_e32 v157, v14, v135
	v_max_i32_e32 v135, 0, v141
	v_fmac_f32_e32 v161, v14, v135
	v_max_i32_e32 v135, 0, v138
	v_fmac_f32_e32 v158, v14, v135
	v_max_i32_e32 v135, 0, v142
	v_fmac_f32_e32 v162, v14, v135
	v_max_i32_e32 v135, 0, v139
	v_mfma_f32_16x16x32_bf16 v[136:139], v[72:75], v[32:35], 0
	v_fmac_f32_e32 v159, v14, v135
	v_max_i32_e32 v135, 0, v143
	v_fmac_f32_e32 v163, v14, v135
	v_mfma_f32_16x16x32_bf16 v[140:143], v[80:83], v[32:35], 0
	v_mfma_f32_16x16x32_bf16 v[136:139], v[76:79], v[36:39], v[136:139]
	v_mfma_f32_16x16x32_bf16 v[140:143], v[84:87], v[36:39], v[140:143]
	s_nop 6
	v_max_i32_e32 v135, 0, v136
	v_fmac_f32_e32 v156, v15, v135
	v_max_i32_e32 v135, 0, v140
	v_fmac_f32_e32 v160, v15, v135
	v_max_i32_e32 v135, 0, v137
	v_fmac_f32_e32 v157, v15, v135
	v_max_i32_e32 v135, 0, v141
	v_fmac_f32_e32 v161, v15, v135
	v_max_i32_e32 v135, 0, v138
	v_fmac_f32_e32 v158, v15, v135
	v_max_i32_e32 v135, 0, v142
	v_fmac_f32_e32 v162, v15, v135
	v_max_i32_e32 v135, 0, v139
	v_mfma_f32_16x16x32_bf16 v[136:139], v[72:75], v[40:43], 0
	v_fmac_f32_e32 v159, v15, v135
	v_max_i32_e32 v135, 0, v143
	v_fmac_f32_e32 v163, v15, v135
	v_mfma_f32_16x16x32_bf16 v[140:143], v[80:83], v[40:43], 0
	v_mfma_f32_16x16x32_bf16 v[136:139], v[76:79], v[44:47], v[136:139]
	v_mfma_f32_16x16x32_bf16 v[140:143], v[84:87], v[44:47], v[140:143]
	s_nop 6
	v_max_i32_e32 v135, 0, v136
	v_fmac_f32_e32 v156, v8, v135
	v_max_i32_e32 v135, 0, v140
	v_fmac_f32_e32 v160, v8, v135
	v_max_i32_e32 v135, 0, v137
	v_fmac_f32_e32 v157, v8, v135
	v_max_i32_e32 v135, 0, v141
	v_fmac_f32_e32 v161, v8, v135
	v_max_i32_e32 v135, 0, v138
	v_fmac_f32_e32 v158, v8, v135
	v_max_i32_e32 v135, 0, v142
	v_fmac_f32_e32 v162, v8, v135
	v_max_i32_e32 v135, 0, v139
	v_mfma_f32_16x16x32_bf16 v[136:139], v[72:75], v[48:51], 0
	v_fmac_f32_e32 v159, v8, v135
	v_max_i32_e32 v135, 0, v143
	v_fmac_f32_e32 v163, v8, v135
	v_mfma_f32_16x16x32_bf16 v[140:143], v[80:83], v[48:51], 0
	v_mfma_f32_16x16x32_bf16 v[136:139], v[76:79], v[52:55], v[136:139]
	v_mfma_f32_16x16x32_bf16 v[140:143], v[84:87], v[52:55], v[140:143]
	s_nop 6
	v_max_i32_e32 v135, 0, v136
	v_fmac_f32_e32 v156, v9, v135
	v_max_i32_e32 v135, 0, v140
	v_fmac_f32_e32 v160, v9, v135
	v_max_i32_e32 v135, 0, v137
	v_fmac_f32_e32 v157, v9, v135
	v_max_i32_e32 v135, 0, v141
	v_fmac_f32_e32 v161, v9, v135
	v_max_i32_e32 v135, 0, v138
	v_fmac_f32_e32 v158, v9, v135
	v_max_i32_e32 v135, 0, v142
	v_fmac_f32_e32 v162, v9, v135
	v_max_i32_e32 v135, 0, v139
	v_mfma_f32_16x16x32_bf16 v[136:139], v[72:75], v[56:59], 0
	v_fmac_f32_e32 v159, v9, v135
	v_max_i32_e32 v135, 0, v143
	v_fmac_f32_e32 v163, v9, v135
	v_mfma_f32_16x16x32_bf16 v[140:143], v[80:83], v[56:59], 0
	v_mfma_f32_16x16x32_bf16 v[136:139], v[76:79], v[60:63], v[136:139]
	v_mfma_f32_16x16x32_bf16 v[140:143], v[84:87], v[60:63], v[140:143]
	s_nop 6
	v_max_i32_e32 v135, 0, v136
	v_fmac_f32_e32 v156, v10, v135
	v_max_i32_e32 v135, 0, v140
	v_fmac_f32_e32 v160, v10, v135
	v_max_i32_e32 v135, 0, v137
	v_fmac_f32_e32 v157, v10, v135
	v_max_i32_e32 v135, 0, v141
	v_fmac_f32_e32 v161, v10, v135
	v_max_i32_e32 v135, 0, v138
	v_fmac_f32_e32 v158, v10, v135
	v_max_i32_e32 v135, 0, v142
	v_fmac_f32_e32 v162, v10, v135
	v_max_i32_e32 v135, 0, v139
	v_mfma_f32_16x16x32_bf16 v[136:139], v[72:75], v[64:67], 0
	v_fmac_f32_e32 v159, v10, v135
	v_max_i32_e32 v135, 0, v143
	v_fmac_f32_e32 v163, v10, v135
	v_mfma_f32_16x16x32_bf16 v[140:143], v[80:83], v[64:67], 0
	v_mfma_f32_16x16x32_bf16 v[136:139], v[76:79], v[68:71], v[136:139]
	v_mfma_f32_16x16x32_bf16 v[140:143], v[84:87], v[68:71], v[140:143]
	s_nop 6
	v_max_i32_e32 v135, 0, v136
	v_fmac_f32_e32 v156, v11, v135
	v_max_i32_e32 v135, 0, v140
	v_fmac_f32_e32 v160, v11, v135
	v_max_i32_e32 v135, 0, v137
	v_fmac_f32_e32 v157, v11, v135
	v_max_i32_e32 v135, 0, v141
	v_fmac_f32_e32 v161, v11, v135
	v_max_i32_e32 v135, 0, v138
	v_fmac_f32_e32 v158, v11, v135
	v_max_i32_e32 v135, 0, v142
	v_fmac_f32_e32 v162, v11, v135
	v_max_i32_e32 v135, 0, v139
	v_fmac_f32_e32 v159, v11, v135
	v_max_i32_e32 v135, 0, v143
	v_fmac_f32_e32 v163, v11, v135
	global_store_dwordx4 v232, v[156:159], s[100:101]
	global_store_dwordx4 v232, v[160:163], s[100:101] offset:16
	v_lshrrev_b32 v135, 22, v156
	v_bfe_u32 v131, v156, 21, 1
	v_mad_u32_u24 v131, v131, s1, 1
	v_lshl_add_u32 v135, v135, 2, v128
	ds_add_u32 v135, v131
	v_lshrrev_b32 v131, 22, v157
	v_bfe_u32 v132, v157, 21, 1
	v_lshl_add_u32 v131, v131, 2, v128
	v_mad_u32_u24 v132, v132, s1, 1
	ds_add_u32 v131, v132
	v_lshrrev_b32 v131, 22, v158
	v_bfe_u32 v132, v158, 21, 1
	v_lshl_add_u32 v131, v131, 2, v128
	v_mad_u32_u24 v132, v132, s1, 1
	ds_add_u32 v131, v132
	v_lshrrev_b32 v131, 22, v159
	v_bfe_u32 v132, v159, 21, 1
	v_lshl_add_u32 v131, v131, 2, v128
	v_mad_u32_u24 v132, v132, s1, 1
	ds_add_u32 v131, v132
	v_lshrrev_b32 v131, 22, v160
	v_bfe_u32 v123, v160, 21, 1
	v_mad_u32_u24 v123, v123, s1, 1
	v_lshl_add_u32 v131, v131, 2, v128
	ds_add_u32 v131, v123
	v_lshrrev_b32 v123, 22, v161
	v_bfe_u32 v124, v161, 21, 1
	v_lshl_add_u32 v123, v123, 2, v128
	v_mad_u32_u24 v124, v124, s1, 1
	ds_add_u32 v123, v124
	v_lshrrev_b32 v123, 22, v162
	v_bfe_u32 v124, v162, 21, 1
	v_lshl_add_u32 v123, v123, 2, v128
	v_mad_u32_u24 v124, v124, s1, 1
	ds_add_u32 v123, v124
	v_lshrrev_b32 v123, 22, v163
	v_bfe_u32 v124, v163, 21, 1
	v_lshl_add_u32 v123, v123, 2, v128
	v_mad_u32_u24 v124, v124, s1, 1
	ds_add_u32 v123, v124
	s_branch .LBB0_1307

.Lpb2_entry:
	s_waitcnt vmcnt(0)
	s_min_i32 s32, s82, 0xf8
	v_lshl_add_u32 v233, s31, 11, v230
	global_load_dwordx4 v[156:159], v233, s[100:101]
	global_load_dwordx4 v[160:163], v233, s[100:101] offset:16
	v_mov_b32_e32 v234, 0x7c000
	global_store_dword v234, v193, s[100:101]
	s_add_i32 s85, s31, 8
	v_lshl_add_u32 v233, s85, 11, v230
	global_load_dwordx4 v[178:181], v233, s[100:101]
	global_load_dwordx4 v[182:185], v233, s[100:101] offset:16
	global_store_dword v234, v193, s[100:101]
.Lpb2_i0:
	s_add_i32 s85, s31, 16
	s_min_i32 s85, s85, 0xff
	v_lshl_add_u32 v233, s85, 11, v230
	global_load_dwordx4 v[236:239], v233, s[100:101]
	global_load_dwordx4 v[240:243], v233, s[100:101] offset:16
	s_waitcnt vmcnt(6)
	v_cmp_ge_f32_e64 s[66:67], v156, v140
	v_cmp_ge_f32_e64 s[50:51], v156, v139
	v_cmp_ge_f32_e32 vcc, v157, v140
	v_cmp_ge_f32_e64 s[52:53], v157, v139
	v_cndmask_b32_e64 v224, 0, 1, s[66:67]
	v_cndmask_b32_e64 v225, 0, 2, vcc
	s_andn2_b64 s[50:51], s[50:51], s[66:67]
	s_andn2_b64 s[52:53], s[52:53], vcc
	v_or_b32_e32 v228, v224, v225
	v_cmp_ge_f32_e64 s[66:67], v158, v140
	v_cmp_ge_f32_e64 s[54:55], v158, v139
	v_cmp_ge_f32_e32 vcc, v159, v140
	v_cmp_ge_f32_e64 s[56:57], v159, v139
	v_cndmask_b32_e64 v224, 0, 4, s[66:67]
	v_cndmask_b32_e64 v225, 0, 8, vcc
	s_andn2_b64 s[54:55], s[54:55], s[66:67]
	s_andn2_b64 s[56:57], s[56:57], vcc
	v_or3_b32 v228, v228, v224, v225
	v_cmp_ge_f32_e64 s[66:67], v160, v140
	v_cmp_ge_f32_e64 s[58:59], v160, v139
	v_cmp_ge_f32_e32 vcc, v161, v140
	v_cmp_ge_f32_e64 s[60:61], v161, v139
	v_cndmask_b32_e64 v224, 0, v201, s[66:67]
	v_cndmask_b32_e64 v225, 0, v200, vcc
	s_andn2_b64 s[58:59], s[58:59], s[66:67]
	s_andn2_b64 s[60:61], s[60:61], vcc
	v_or3_b32 v228, v228, v224, v225
	v_cmp_ge_f32_e64 s[66:67], v162, v140
	v_cmp_ge_f32_e64 s[62:63], v162, v139
	v_cmp_ge_f32_e32 vcc, v163, v140
	v_cmp_ge_f32_e64 s[64:65], v163, v139
	v_cndmask_b32_e64 v224, 0, v199, s[66:67]
	v_cndmask_b32_e64 v225, 0, v198, vcc
	s_andn2_b64 s[62:63], s[62:63], s[66:67]
	s_andn2_b64 s[64:65], s[64:65], vcc
	v_or3_b32 v228, v228, v224, v225
	v_add_u32_e32 v226, s74, v124
	v_mov_b32_e32 v227, s96
	s_mov_b64 s[14:15], exec
	s_mov_b64 exec, s[50:51]
	v_ashrrev_i32_e32 v206, 31, v156
	v_xor_b32_e32 v206, v206, v156
	v_lshrrev_b32_e32 v222, 9, v206
	v_lshrrev_b32_e32 v223, 6, v206
	v_and_b32_e32 v222, 0xffc, v222
	v_and_b32_e32 v223, 16, v223
	v_add_u32_e32 v222, v128, v222
	v_lshlrev_b32_e64 v223, v223, 1
	ds_add_u32 v222, v223
	s_mov_b64 exec, s[52:53]
	v_ashrrev_i32_e32 v207, 31, v157
	v_xor_b32_e32 v207, v207, v157
	v_lshrrev_b32_e32 v222, 9, v207
	v_lshrrev_b32_e32 v223, 6, v207
	v_and_b32_e32 v222, 0xffc, v222
	v_and_b32_e32 v223, 16, v223
	v_add_u32_e32 v222, v128, v222
	v_lshlrev_b32_e64 v223, v223, 1
	ds_add_u32 v222, v223
	s_mov_b64 exec, s[54:55]
	v_ashrrev_i32_e32 v208, 31, v158
	v_xor_b32_e32 v208, v208, v158
	v_lshrrev_b32_e32 v222, 9, v208
	v_lshrrev_b32_e32 v223, 6, v208
	v_and_b32_e32 v222, 0xffc, v222
	v_and_b32_e32 v223, 16, v223
	v_add_u32_e32 v222, v128, v222
	v_lshlrev_b32_e64 v223, v223, 1
	ds_add_u32 v222, v223
	s_mov_b64 exec, s[56:57]
	v_ashrrev_i32_e32 v209, 31, v159
	v_xor_b32_e32 v209, v209, v159
	v_lshrrev_b32_e32 v222, 9, v209
	v_lshrrev_b32_e32 v223, 6, v209
	v_and_b32_e32 v222, 0xffc, v222
	v_and_b32_e32 v223, 16, v223
	v_add_u32_e32 v222, v128, v222
	v_lshlrev_b32_e64 v223, v223, 1
	ds_add_u32 v222, v223
	s_mov_b64 exec, s[58:59]
	v_ashrrev_i32_e32 v210, 31, v160
	v_xor_b32_e32 v210, v210, v160
	v_lshrrev_b32_e32 v222, 9, v210
	v_lshrrev_b32_e32 v223, 6, v210
	v_and_b32_e32 v222, 0xffc, v222
	v_and_b32_e32 v223, 16, v223
	v_add_u32_e32 v222, v128, v222
	v_lshlrev_b32_e64 v223, v223, 1
	ds_add_u32 v222, v223
	s_mov_b64 exec, s[60:61]
	v_ashrrev_i32_e32 v211, 31, v161
	v_xor_b32_e32 v211, v211, v161
	v_lshrrev_b32_e32 v222, 9, v211
	v_lshrrev_b32_e32 v223, 6, v211
	v_and_b32_e32 v222, 0xffc, v222
	v_and_b32_e32 v223, 16, v223
	v_add_u32_e32 v222, v128, v222
	v_lshlrev_b32_e64 v223, v223, 1
	ds_add_u32 v222, v223
	s_mov_b64 exec, s[62:63]
	v_ashrrev_i32_e32 v212, 31, v162
	v_xor_b32_e32 v212, v212, v162
	v_lshrrev_b32_e32 v222, 9, v212
	v_lshrrev_b32_e32 v223, 6, v212
	v_and_b32_e32 v222, 0xffc, v222
	v_and_b32_e32 v223, 16, v223
	v_add_u32_e32 v222, v128, v222
	v_lshlrev_b32_e64 v223, v223, 1
	ds_add_u32 v222, v223
	s_mov_b64 exec, s[64:65]
	v_ashrrev_i32_e32 v213, 31, v163
	v_xor_b32_e32 v213, v213, v163
	v_lshrrev_b32_e32 v222, 9, v213
	v_lshrrev_b32_e32 v223, 6, v213
	v_and_b32_e32 v222, 0xffc, v222
	v_and_b32_e32 v223, 16, v223
	v_add_u32_e32 v222, v128, v222
	v_lshlrev_b32_e64 v223, v223, 1
	ds_add_u32 v222, v223
	s_waitcnt lgkmcnt(6)
	s_mov_b64 exec, s[50:51]
	ds_add_rtn_u32 v214, v142, v193
	s_mov_b64 exec, s[52:53]
	ds_add_rtn_u32 v215, v142, v193
	s_mov_b64 exec, s[54:55]
	ds_add_rtn_u32 v216, v142, v193
	s_mov_b64 exec, s[56:57]
	ds_add_rtn_u32 v217, v142, v193
	s_mov_b64 exec, s[58:59]
	ds_add_rtn_u32 v218, v142, v193
	s_mov_b64 exec, s[60:61]
	ds_add_rtn_u32 v219, v142, v193
	s_mov_b64 exec, s[62:63]
	ds_add_rtn_u32 v220, v142, v193
	s_mov_b64 exec, s[64:65]
	ds_add_rtn_u32 v221, v142, v193
	s_waitcnt lgkmcnt(0)
	s_mov_b64 exec, s[50:51]
	v_cmp_lt_u32_e64 s[66:67], s0, v214
	v_bfe_u32 v224, v206, 10, 11
	v_add_u32_e32 v225, 0x0, v226
	v_lshl_add_u32 v222, v214, 2, v141
	v_add_u32_e32 v224, v225, v224
	s_andn2_b64 exec, exec, s[66:67]
	ds_write_b32 v222, v224
	s_mov_b64 exec, s[66:67]
	ds_write_b32 v227, v193
	s_mov_b64 exec, s[52:53]
	v_cmp_lt_u32_e64 s[66:67], s0, v215
	v_bfe_u32 v224, v207, 10, 11
	v_add_u32_e32 v225, 0x800, v226
	v_lshl_add_u32 v222, v215, 2, v141
	v_add_u32_e32 v224, v225, v224
	s_andn2_b64 exec, exec, s[66:67]
	ds_write_b32 v222, v224
	s_mov_b64 exec, s[66:67]
	ds_write_b32 v227, v193
	s_mov_b64 exec, s[54:55]
	v_cmp_lt_u32_e64 s[66:67], s0, v216
	v_bfe_u32 v224, v208, 10, 11
	v_add_u32_e32 v225, 0x1000, v226
	v_lshl_add_u32 v222, v216, 2, v141
	v_add_u32_e32 v224, v225, v224
	s_andn2_b64 exec, exec, s[66:67]
	ds_write_b32 v222, v224
	s_mov_b64 exec, s[66:67]
	ds_write_b32 v227, v193
	s_mov_b64 exec, s[56:57]
	v_cmp_lt_u32_e64 s[66:67], s0, v217
	v_bfe_u32 v224, v209, 10, 11
	v_add_u32_e32 v225, 0x1800, v226
	v_lshl_add_u32 v222, v217, 2, v141
	v_add_u32_e32 v224, v225, v224
	s_andn2_b64 exec, exec, s[66:67]
	ds_write_b32 v222, v224
	s_mov_b64 exec, s[66:67]
	ds_write_b32 v227, v193
	s_waitcnt lgkmcnt(4)
	s_mov_b64 exec, s[58:59]
	v_cmp_lt_u32_e64 s[66:67], s0, v218
	v_bfe_u32 v224, v210, 10, 11
	v_add_u32_e32 v225, 0x8000, v226
	v_lshl_add_u32 v222, v218, 2, v141
	v_add_u32_e32 v224, v225, v224
	s_andn2_b64 exec, exec, s[66:67]
	ds_write_b32 v222, v224
	s_mov_b64 exec, s[66:67]
	ds_write_b32 v227, v193
	s_mov_b64 exec, s[60:61]
	v_cmp_lt_u32_e64 s[66:67], s0, v219
	v_bfe_u32 v224, v211, 10, 11
	v_add_u32_e32 v225, 0x8800, v226
	v_lshl_add_u32 v222, v219, 2, v141
	v_add_u32_e32 v224, v225, v224
	s_andn2_b64 exec, exec, s[66:67]
	ds_write_b32 v222, v224
	s_mov_b64 exec, s[66:67]
	ds_write_b32 v227, v193
	s_mov_b64 exec, s[62:63]
	v_cmp_lt_u32_e64 s[66:67], s0, v220
	v_bfe_u32 v224, v212, 10, 11
	v_add_u32_e32 v225, 0x9000, v226
	v_lshl_add_u32 v222, v220, 2, v141
	v_add_u32_e32 v224, v225, v224
	s_andn2_b64 exec, exec, s[66:67]
	ds_write_b32 v222, v224
	s_mov_b64 exec, s[66:67]
	ds_write_b32 v227, v193
	s_mov_b64 exec, s[64:65]
	v_cmp_lt_u32_e64 s[66:67], s0, v221
	v_bfe_u32 v224, v213, 10, 11
	v_add_u32_e32 v225, 0x9800, v226
	v_lshl_add_u32 v222, v221, 2, v141
	v_add_u32_e32 v224, v225, v224
	s_andn2_b64 exec, exec, s[66:67]
	ds_write_b32 v222, v224
	s_mov_b64 exec, s[66:67]
	ds_write_b32 v227, v193
	s_mov_b64 exec, s[14:15]
	v_mov_b32_e32 v104, v228
	v_lshlrev_b32_e32 v104, v143, v104
	ds_bpermute_b32 v105, v144, v104
	s_waitcnt lgkmcnt(0)
	v_or_b32_e32 v104, v105, v104
	ds_bpermute_b32 v105, v145, v104
	s_and_saveexec_b64 s[14:15], s[38:39]
	s_waitcnt lgkmcnt(0)
	v_or_b32_e32 v106, v104, v105
	v_lshl_add_u64 v[104:105], v[122:123], 0, s[74:75]
	v_add_co_u32_e32 v104, vcc, 0x3f700000, v104
	s_nop 1
	v_addc_co_u32_e32 v105, vcc, 0, v105, vcc
	global_store_dword v[104:105], v106, off
	s_or_b64 exec, exec, s[14:15]
	s_add_u32 s74, s74, 0x80000
	s_addc_u32 s75, s75, 0
	s_add_i32 s31, s31, 8
	s_cmp_ge_i32 s31, s32
	s_cbranch_scc1 .Lpb2_done
.Lpb2_i1:
	s_add_i32 s85, s31, 16
	s_min_i32 s85, s85, 0xff
	v_lshl_add_u32 v233, s85, 11, v230
	global_load_dwordx4 v[156:159], v233, s[100:101]
	global_load_dwordx4 v[160:163], v233, s[100:101] offset:16
	s_waitcnt vmcnt(6)
	v_cmp_ge_f32_e64 s[66:67], v178, v140
	v_cmp_ge_f32_e64 s[50:51], v178, v139
	v_cmp_ge_f32_e32 vcc, v179, v140
	v_cmp_ge_f32_e64 s[52:53], v179, v139
	v_cndmask_b32_e64 v224, 0, 1, s[66:67]
	v_cndmask_b32_e64 v225, 0, 2, vcc
	s_andn2_b64 s[50:51], s[50:51], s[66:67]
	s_andn2_b64 s[52:53], s[52:53], vcc
	v_or_b32_e32 v228, v224, v225
	v_cmp_ge_f32_e64 s[66:67], v180, v140
	v_cmp_ge_f32_e64 s[54:55], v180, v139
	v_cmp_ge_f32_e32 vcc, v181, v140
	v_cmp_ge_f32_e64 s[56:57], v181, v139
	v_cndmask_b32_e64 v224, 0, 4, s[66:67]
	v_cndmask_b32_e64 v225, 0, 8, vcc
	s_andn2_b64 s[54:55], s[54:55], s[66:67]
	s_andn2_b64 s[56:57], s[56:57], vcc
	v_or3_b32 v228, v228, v224, v225
	v_cmp_ge_f32_e64 s[66:67], v182, v140
	v_cmp_ge_f32_e64 s[58:59], v182, v139
	v_cmp_ge_f32_e32 vcc, v183, v140
	v_cmp_ge_f32_e64 s[60:61], v183, v139
	v_cndmask_b32_e64 v224, 0, v201, s[66:67]
	v_cndmask_b32_e64 v225, 0, v200, vcc
	s_andn2_b64 s[58:59], s[58:59], s[66:67]
	s_andn2_b64 s[60:61], s[60:61], vcc
	v_or3_b32 v228, v228, v224, v225
	v_cmp_ge_f32_e64 s[66:67], v184, v140
	v_cmp_ge_f32_e64 s[62:63], v184, v139
	v_cmp_ge_f32_e32 vcc, v185, v140
	v_cmp_ge_f32_e64 s[64:65], v185, v139
	v_cndmask_b32_e64 v224, 0, v199, s[66:67]
	v_cndmask_b32_e64 v225, 0, v198, vcc
	s_andn2_b64 s[62:63], s[62:63], s[66:67]
	s_andn2_b64 s[64:65], s[64:65], vcc
	v_or3_b32 v228, v228, v224, v225
	v_add_u32_e32 v226, s74, v124
	v_mov_b32_e32 v227, s96
	s_mov_b64 s[14:15], exec
	s_mov_b64 exec, s[50:51]
	v_ashrrev_i32_e32 v206, 31, v178
	v_xor_b32_e32 v206, v206, v178
	v_lshrrev_b32_e32 v222, 9, v206
	v_lshrrev_b32_e32 v223, 6, v206
	v_and_b32_e32 v222, 0xffc, v222
	v_and_b32_e32 v223, 16, v223
	v_add_u32_e32 v222, v128, v222
	v_lshlrev_b32_e64 v223, v223, 1
	ds_add_u32 v222, v223
	s_mov_b64 exec, s[52:53]
	v_ashrrev_i32_e32 v207, 31, v179
	v_xor_b32_e32 v207, v207, v179
	v_lshrrev_b32_e32 v222, 9, v207
	v_lshrrev_b32_e32 v223, 6, v207
	v_and_b32_e32 v222, 0xffc, v222
	v_and_b32_e32 v223, 16, v223
	v_add_u32_e32 v222, v128, v222
	v_lshlrev_b32_e64 v223, v223, 1
	ds_add_u32 v222, v223
	s_mov_b64 exec, s[54:55]
	v_ashrrev_i32_e32 v208, 31, v180
	v_xor_b32_e32 v208, v208, v180
	v_lshrrev_b32_e32 v222, 9, v208
	v_lshrrev_b32_e32 v223, 6, v208
	v_and_b32_e32 v222, 0xffc, v222
	v_and_b32_e32 v223, 16, v223
	v_add_u32_e32 v222, v128, v222
	v_lshlrev_b32_e64 v223, v223, 1
	ds_add_u32 v222, v223
	s_mov_b64 exec, s[56:57]
	v_ashrrev_i32_e32 v209, 31, v181
	v_xor_b32_e32 v209, v209, v181
	v_lshrrev_b32_e32 v222, 9, v209
	v_lshrrev_b32_e32 v223, 6, v209
	v_and_b32_e32 v222, 0xffc, v222
	v_and_b32_e32 v223, 16, v223
	v_add_u32_e32 v222, v128, v222
	v_lshlrev_b32_e64 v223, v223, 1
	ds_add_u32 v222, v223
	s_mov_b64 exec, s[58:59]
	v_ashrrev_i32_e32 v210, 31, v182
	v_xor_b32_e32 v210, v210, v182
	v_lshrrev_b32_e32 v222, 9, v210
	v_lshrrev_b32_e32 v223, 6, v210
	v_and_b32_e32 v222, 0xffc, v222
	v_and_b32_e32 v223, 16, v223
	v_add_u32_e32 v222, v128, v222
	v_lshlrev_b32_e64 v223, v223, 1
	ds_add_u32 v222, v223
	s_mov_b64 exec, s[60:61]
	v_ashrrev_i32_e32 v211, 31, v183
	v_xor_b32_e32 v211, v211, v183
	v_lshrrev_b32_e32 v222, 9, v211
	v_lshrrev_b32_e32 v223, 6, v211
	v_and_b32_e32 v222, 0xffc, v222
	v_and_b32_e32 v223, 16, v223
	v_add_u32_e32 v222, v128, v222
	v_lshlrev_b32_e64 v223, v223, 1
	ds_add_u32 v222, v223
	s_mov_b64 exec, s[62:63]
	v_ashrrev_i32_e32 v212, 31, v184
	v_xor_b32_e32 v212, v212, v184
	v_lshrrev_b32_e32 v222, 9, v212
	v_lshrrev_b32_e32 v223, 6, v212
	v_and_b32_e32 v222, 0xffc, v222
	v_and_b32_e32 v223, 16, v223
	v_add_u32_e32 v222, v128, v222
	v_lshlrev_b32_e64 v223, v223, 1
	ds_add_u32 v222, v223
	s_mov_b64 exec, s[64:65]
	v_ashrrev_i32_e32 v213, 31, v185
	v_xor_b32_e32 v213, v213, v185
	v_lshrrev_b32_e32 v222, 9, v213
	v_lshrrev_b32_e32 v223, 6, v213
	v_and_b32_e32 v222, 0xffc, v222
	v_and_b32_e32 v223, 16, v223
	v_add_u32_e32 v222, v128, v222
	v_lshlrev_b32_e64 v223, v223, 1
	ds_add_u32 v222, v223
	s_waitcnt lgkmcnt(6)
	s_mov_b64 exec, s[50:51]
	ds_add_rtn_u32 v214, v142, v193
	s_mov_b64 exec, s[52:53]
	ds_add_rtn_u32 v215, v142, v193
	s_mov_b64 exec, s[54:55]
	ds_add_rtn_u32 v216, v142, v193
	s_mov_b64 exec, s[56:57]
	ds_add_rtn_u32 v217, v142, v193
	s_mov_b64 exec, s[58:59]
	ds_add_rtn_u32 v218, v142, v193
	s_mov_b64 exec, s[60:61]
	ds_add_rtn_u32 v219, v142, v193
	s_mov_b64 exec, s[62:63]
	ds_add_rtn_u32 v220, v142, v193
	s_mov_b64 exec, s[64:65]
	ds_add_rtn_u32 v221, v142, v193
	s_waitcnt lgkmcnt(0)
	s_mov_b64 exec, s[50:51]
	v_cmp_lt_u32_e64 s[66:67], s0, v214
	v_bfe_u32 v224, v206, 10, 11
	v_add_u32_e32 v225, 0x0, v226
	v_lshl_add_u32 v222, v214, 2, v141
	v_add_u32_e32 v224, v225, v224
	s_andn2_b64 exec, exec, s[66:67]
	ds_write_b32 v222, v224
	s_mov_b64 exec, s[66:67]
	ds_write_b32 v227, v193
	s_mov_b64 exec, s[52:53]
	v_cmp_lt_u32_e64 s[66:67], s0, v215
	v_bfe_u32 v224, v207, 10, 11
	v_add_u32_e32 v225, 0x800, v226
	v_lshl_add_u32 v222, v215, 2, v141
	v_add_u32_e32 v224, v225, v224
	s_andn2_b64 exec, exec, s[66:67]
	ds_write_b32 v222, v224
	s_mov_b64 exec, s[66:67]
	ds_write_b32 v227, v193
	s_mov_b64 exec, s[54:55]
	v_cmp_lt_u32_e64 s[66:67], s0, v216
	v_bfe_u32 v224, v208, 10, 11
	v_add_u32_e32 v225, 0x1000, v226
	v_lshl_add_u32 v222, v216, 2, v141
	v_add_u32_e32 v224, v225, v224
	s_andn2_b64 exec, exec, s[66:67]
	ds_write_b32 v222, v224
	s_mov_b64 exec, s[66:67]
	ds_write_b32 v227, v193
	s_mov_b64 exec, s[56:57]
	v_cmp_lt_u32_e64 s[66:67], s0, v217
	v_bfe_u32 v224, v209, 10, 11
	v_add_u32_e32 v225, 0x1800, v226
	v_lshl_add_u32 v222, v217, 2, v141
	v_add_u32_e32 v224, v225, v224
	s_andn2_b64 exec, exec, s[66:67]
	ds_write_b32 v222, v224
	s_mov_b64 exec, s[66:67]
	ds_write_b32 v227, v193
	s_waitcnt lgkmcnt(4)
	s_mov_b64 exec, s[58:59]
	v_cmp_lt_u32_e64 s[66:67], s0, v218
	v_bfe_u32 v224, v210, 10, 11
	v_add_u32_e32 v225, 0x8000, v226
	v_lshl_add_u32 v222, v218, 2, v141
	v_add_u32_e32 v224, v225, v224
	s_andn2_b64 exec, exec, s[66:67]
	ds_write_b32 v222, v224
	s_mov_b64 exec, s[66:67]
	ds_write_b32 v227, v193
	s_mov_b64 exec, s[60:61]
	v_cmp_lt_u32_e64 s[66:67], s0, v219
	v_bfe_u32 v224, v211, 10, 11
	v_add_u32_e32 v225, 0x8800, v226
	v_lshl_add_u32 v222, v219, 2, v141
	v_add_u32_e32 v224, v225, v224
	s_andn2_b64 exec, exec, s[66:67]
	ds_write_b32 v222, v224
	s_mov_b64 exec, s[66:67]
	ds_write_b32 v227, v193
	s_mov_b64 exec, s[62:63]
	v_cmp_lt_u32_e64 s[66:67], s0, v220
	v_bfe_u32 v224, v212, 10, 11
	v_add_u32_e32 v225, 0x9000, v226
	v_lshl_add_u32 v222, v220, 2, v141
	v_add_u32_e32 v224, v225, v224
	s_andn2_b64 exec, exec, s[66:67]
	ds_write_b32 v222, v224
	s_mov_b64 exec, s[66:67]
	ds_write_b32 v227, v193
	s_mov_b64 exec, s[64:65]
	v_cmp_lt_u32_e64 s[66:67], s0, v221
	v_bfe_u32 v224, v213, 10, 11
	v_add_u32_e32 v225, 0x9800, v226
	v_lshl_add_u32 v222, v221, 2, v141
	v_add_u32_e32 v224, v225, v224
	s_andn2_b64 exec, exec, s[66:67]
	ds_write_b32 v222, v224
	s_mov_b64 exec, s[66:67]
	ds_write_b32 v227, v193
	s_mov_b64 exec, s[14:15]
	v_mov_b32_e32 v104, v228
	v_lshlrev_b32_e32 v104, v143, v104
	ds_bpermute_b32 v105, v144, v104
	s_waitcnt lgkmcnt(0)
	v_or_b32_e32 v104, v105, v104
	ds_bpermute_b32 v105, v145, v104
	s_and_saveexec_b64 s[14:15], s[38:39]
	s_waitcnt lgkmcnt(0)
	v_or_b32_e32 v106, v104, v105
	v_lshl_add_u64 v[104:105], v[122:123], 0, s[74:75]
	v_add_co_u32_e32 v104, vcc, 0x3f700000, v104
	s_nop 1
	v_addc_co_u32_e32 v105, vcc, 0, v105, vcc
	global_store_dword v[104:105], v106, off
	s_or_b64 exec, exec, s[14:15]
	s_add_u32 s74, s74, 0x80000
	s_addc_u32 s75, s75, 0
	s_add_i32 s31, s31, 8
	s_cmp_ge_i32 s31, s32
	s_cbranch_scc1 .Lpb2_done
.Lpb2_i2:
	s_add_i32 s85, s31, 16
	s_min_i32 s85, s85, 0xff
	v_lshl_add_u32 v233, s85, 11, v230
	global_load_dwordx4 v[178:181], v233, s[100:101]
	global_load_dwordx4 v[182:185], v233, s[100:101] offset:16
	s_waitcnt vmcnt(6)
	v_cmp_ge_f32_e64 s[66:67], v236, v140
	v_cmp_ge_f32_e64 s[50:51], v236, v139
	v_cmp_ge_f32_e32 vcc, v237, v140
	v_cmp_ge_f32_e64 s[52:53], v237, v139
	v_cndmask_b32_e64 v224, 0, 1, s[66:67]
	v_cndmask_b32_e64 v225, 0, 2, vcc
	s_andn2_b64 s[50:51], s[50:51], s[66:67]
	s_andn2_b64 s[52:53], s[52:53], vcc
	v_or_b32_e32 v228, v224, v225
	v_cmp_ge_f32_e64 s[66:67], v238, v140
	v_cmp_ge_f32_e64 s[54:55], v238, v139
	v_cmp_ge_f32_e32 vcc, v239, v140
	v_cmp_ge_f32_e64 s[56:57], v239, v139
	v_cndmask_b32_e64 v224, 0, 4, s[66:67]
	v_cndmask_b32_e64 v225, 0, 8, vcc
	s_andn2_b64 s[54:55], s[54:55], s[66:67]
	s_andn2_b64 s[56:57], s[56:57], vcc
	v_or3_b32 v228, v228, v224, v225
	v_cmp_ge_f32_e64 s[66:67], v240, v140
	v_cmp_ge_f32_e64 s[58:59], v240, v139
	v_cmp_ge_f32_e32 vcc, v241, v140
	v_cmp_ge_f32_e64 s[60:61], v241, v139
	v_cndmask_b32_e64 v224, 0, v201, s[66:67]
	v_cndmask_b32_e64 v225, 0, v200, vcc
	s_andn2_b64 s[58:59], s[58:59], s[66:67]
	s_andn2_b64 s[60:61], s[60:61], vcc
	v_or3_b32 v228, v228, v224, v225
	v_cmp_ge_f32_e64 s[66:67], v242, v140
	v_cmp_ge_f32_e64 s[62:63], v242, v139
	v_cmp_ge_f32_e32 vcc, v243, v140
	v_cmp_ge_f32_e64 s[64:65], v243, v139
	v_cndmask_b32_e64 v224, 0, v199, s[66:67]
	v_cndmask_b32_e64 v225, 0, v198, vcc
	s_andn2_b64 s[62:63], s[62:63], s[66:67]
	s_andn2_b64 s[64:65], s[64:65], vcc
	v_or3_b32 v228, v228, v224, v225
	v_add_u32_e32 v226, s74, v124
	v_mov_b32_e32 v227, s96
	s_mov_b64 s[14:15], exec
	s_mov_b64 exec, s[50:51]
	v_ashrrev_i32_e32 v206, 31, v236
	v_xor_b32_e32 v206, v206, v236
	v_lshrrev_b32_e32 v222, 9, v206
	v_lshrrev_b32_e32 v223, 6, v206
	v_and_b32_e32 v222, 0xffc, v222
	v_and_b32_e32 v223, 16, v223
	v_add_u32_e32 v222, v128, v222
	v_lshlrev_b32_e64 v223, v223, 1
	ds_add_u32 v222, v223
	s_mov_b64 exec, s[52:53]
	v_ashrrev_i32_e32 v207, 31, v237
	v_xor_b32_e32 v207, v207, v237
	v_lshrrev_b32_e32 v222, 9, v207
	v_lshrrev_b32_e32 v223, 6, v207
	v_and_b32_e32 v222, 0xffc, v222
	v_and_b32_e32 v223, 16, v223
	v_add_u32_e32 v222, v128, v222
	v_lshlrev_b32_e64 v223, v223, 1
	ds_add_u32 v222, v223
	s_mov_b64 exec, s[54:55]
	v_ashrrev_i32_e32 v208, 31, v238
	v_xor_b32_e32 v208, v208, v238
	v_lshrrev_b32_e32 v222, 9, v208
	v_lshrrev_b32_e32 v223, 6, v208
	v_and_b32_e32 v222, 0xffc, v222
	v_and_b32_e32 v223, 16, v223
	v_add_u32_e32 v222, v128, v222
	v_lshlrev_b32_e64 v223, v223, 1
	ds_add_u32 v222, v223
	s_mov_b64 exec, s[56:57]
	v_ashrrev_i32_e32 v209, 31, v239
	v_xor_b32_e32 v209, v209, v239
	v_lshrrev_b32_e32 v222, 9, v209
	v_lshrrev_b32_e32 v223, 6, v209
	v_and_b32_e32 v222, 0xffc, v222
	v_and_b32_e32 v223, 16, v223
	v_add_u32_e32 v222, v128, v222
	v_lshlrev_b32_e64 v223, v223, 1
	ds_add_u32 v222, v223
	s_mov_b64 exec, s[58:59]
	v_ashrrev_i32_e32 v210, 31, v240
	v_xor_b32_e32 v210, v210, v240
	v_lshrrev_b32_e32 v222, 9, v210
	v_lshrrev_b32_e32 v223, 6, v210
	v_and_b32_e32 v222, 0xffc, v222
	v_and_b32_e32 v223, 16, v223
	v_add_u32_e32 v222, v128, v222
	v_lshlrev_b32_e64 v223, v223, 1
	ds_add_u32 v222, v223
	s_mov_b64 exec, s[60:61]
	v_ashrrev_i32_e32 v211, 31, v241
	v_xor_b32_e32 v211, v211, v241
	v_lshrrev_b32_e32 v222, 9, v211
	v_lshrrev_b32_e32 v223, 6, v211
	v_and_b32_e32 v222, 0xffc, v222
	v_and_b32_e32 v223, 16, v223
	v_add_u32_e32 v222, v128, v222
	v_lshlrev_b32_e64 v223, v223, 1
	ds_add_u32 v222, v223
	s_mov_b64 exec, s[62:63]
	v_ashrrev_i32_e32 v212, 31, v242
	v_xor_b32_e32 v212, v212, v242
	v_lshrrev_b32_e32 v222, 9, v212
	v_lshrrev_b32_e32 v223, 6, v212
	v_and_b32_e32 v222, 0xffc, v222
	v_and_b32_e32 v223, 16, v223
	v_add_u32_e32 v222, v128, v222
	v_lshlrev_b32_e64 v223, v223, 1
	ds_add_u32 v222, v223
	s_mov_b64 exec, s[64:65]
	v_ashrrev_i32_e32 v213, 31, v243
	v_xor_b32_e32 v213, v213, v243
	v_lshrrev_b32_e32 v222, 9, v213
	v_lshrrev_b32_e32 v223, 6, v213
	v_and_b32_e32 v222, 0xffc, v222
	v_and_b32_e32 v223, 16, v223
	v_add_u32_e32 v222, v128, v222
	v_lshlrev_b32_e64 v223, v223, 1
	ds_add_u32 v222, v223
	s_waitcnt lgkmcnt(6)
	s_mov_b64 exec, s[50:51]
	ds_add_rtn_u32 v214, v142, v193
	s_mov_b64 exec, s[52:53]
	ds_add_rtn_u32 v215, v142, v193
	s_mov_b64 exec, s[54:55]
	ds_add_rtn_u32 v216, v142, v193
	s_mov_b64 exec, s[56:57]
	ds_add_rtn_u32 v217, v142, v193
	s_mov_b64 exec, s[58:59]
	ds_add_rtn_u32 v218, v142, v193
	s_mov_b64 exec, s[60:61]
	ds_add_rtn_u32 v219, v142, v193
	s_mov_b64 exec, s[62:63]
	ds_add_rtn_u32 v220, v142, v193
	s_mov_b64 exec, s[64:65]
	ds_add_rtn_u32 v221, v142, v193
	s_waitcnt lgkmcnt(0)
	s_mov_b64 exec, s[50:51]
	v_cmp_lt_u32_e64 s[66:67], s0, v214
	v_bfe_u32 v224, v206, 10, 11
	v_add_u32_e32 v225, 0x0, v226
	v_lshl_add_u32 v222, v214, 2, v141
	v_add_u32_e32 v224, v225, v224
	s_andn2_b64 exec, exec, s[66:67]
	ds_write_b32 v222, v224
	s_mov_b64 exec, s[66:67]
	ds_write_b32 v227, v193
	s_mov_b64 exec, s[52:53]
	v_cmp_lt_u32_e64 s[66:67], s0, v215
	v_bfe_u32 v224, v207, 10, 11
	v_add_u32_e32 v225, 0x800, v226
	v_lshl_add_u32 v222, v215, 2, v141
	v_add_u32_e32 v224, v225, v224
	s_andn2_b64 exec, exec, s[66:67]
	ds_write_b32 v222, v224
	s_mov_b64 exec, s[66:67]
	ds_write_b32 v227, v193
	s_mov_b64 exec, s[54:55]
	v_cmp_lt_u32_e64 s[66:67], s0, v216
	v_bfe_u32 v224, v208, 10, 11
	v_add_u32_e32 v225, 0x1000, v226
	v_lshl_add_u32 v222, v216, 2, v141
	v_add_u32_e32 v224, v225, v224
	s_andn2_b64 exec, exec, s[66:67]
	ds_write_b32 v222, v224
	s_mov_b64 exec, s[66:67]
	ds_write_b32 v227, v193
	s_mov_b64 exec, s[56:57]
	v_cmp_lt_u32_e64 s[66:67], s0, v217
	v_bfe_u32 v224, v209, 10, 11
	v_add_u32_e32 v225, 0x1800, v226
	v_lshl_add_u32 v222, v217, 2, v141
	v_add_u32_e32 v224, v225, v224
	s_andn2_b64 exec, exec, s[66:67]
	ds_write_b32 v222, v224
	s_mov_b64 exec, s[66:67]
	ds_write_b32 v227, v193
	s_waitcnt lgkmcnt(4)
	s_mov_b64 exec, s[58:59]
	v_cmp_lt_u32_e64 s[66:67], s0, v218
	v_bfe_u32 v224, v210, 10, 11
	v_add_u32_e32 v225, 0x8000, v226
	v_lshl_add_u32 v222, v218, 2, v141
	v_add_u32_e32 v224, v225, v224
	s_andn2_b64 exec, exec, s[66:67]
	ds_write_b32 v222, v224
	s_mov_b64 exec, s[66:67]
	ds_write_b32 v227, v193
	s_mov_b64 exec, s[60:61]
	v_cmp_lt_u32_e64 s[66:67], s0, v219
	v_bfe_u32 v224, v211, 10, 11
	v_add_u32_e32 v225, 0x8800, v226
	v_lshl_add_u32 v222, v219, 2, v141
	v_add_u32_e32 v224, v225, v224
	s_andn2_b64 exec, exec, s[66:67]
	ds_write_b32 v222, v224
	s_mov_b64 exec, s[66:67]
	ds_write_b32 v227, v193
	s_mov_b64 exec, s[62:63]
	v_cmp_lt_u32_e64 s[66:67], s0, v220
	v_bfe_u32 v224, v212, 10, 11
	v_add_u32_e32 v225, 0x9000, v226
	v_lshl_add_u32 v222, v220, 2, v141
	v_add_u32_e32 v224, v225, v224
	s_andn2_b64 exec, exec, s[66:67]
	ds_write_b32 v222, v224
	s_mov_b64 exec, s[66:67]
	ds_write_b32 v227, v193
	s_mov_b64 exec, s[64:65]
	v_cmp_lt_u32_e64 s[66:67], s0, v221
	v_bfe_u32 v224, v213, 10, 11
	v_add_u32_e32 v225, 0x9800, v226
	v_lshl_add_u32 v222, v221, 2, v141
	v_add_u32_e32 v224, v225, v224
	s_andn2_b64 exec, exec, s[66:67]
	ds_write_b32 v222, v224
	s_mov_b64 exec, s[66:67]
	ds_write_b32 v227, v193
	s_mov_b64 exec, s[14:15]
	v_mov_b32_e32 v104, v228
	v_lshlrev_b32_e32 v104, v143, v104
	ds_bpermute_b32 v105, v144, v104
	s_waitcnt lgkmcnt(0)
	v_or_b32_e32 v104, v105, v104
	ds_bpermute_b32 v105, v145, v104
	s_and_saveexec_b64 s[14:15], s[38:39]
	s_waitcnt lgkmcnt(0)
	v_or_b32_e32 v106, v104, v105
	v_lshl_add_u64 v[104:105], v[122:123], 0, s[74:75]
	v_add_co_u32_e32 v104, vcc, 0x3f700000, v104
	s_nop 1
	v_addc_co_u32_e32 v105, vcc, 0, v105, vcc
	global_store_dword v[104:105], v106, off
	s_or_b64 exec, exec, s[14:15]
	s_add_u32 s74, s74, 0x80000
	s_addc_u32 s75, s75, 0
	s_add_i32 s31, s31, 8
	s_cmp_ge_i32 s31, s32
	s_cbranch_scc0 .Lpb2_i0
.Lpb2_done:
	s_cmp_ge_i32 s31, s82
	s_cbranch_scc1 .LBB0_1523
	s_min_i32 s14, s31, s72
	v_lshl_or_b32 v104, s14, 5, v125
	v_ashrrev_i32_e32 v105, 31, v104
	v_lshlrev_b64 v[104:105], 7, v[104:105]
	v_sub_u32_e32 v104, v104, v229
	v_lshl_add_u64 v[104:105], v[120:121], 0, v[104:105]
	global_load_dwordx4 v[116:119], v[104:105], off
	global_load_dwordx4 v[108:111], v[104:105], off offset:1024
	global_load_dwordx4 v[112:115], v[104:105], off offset:2048
	s_nop 0
	global_load_dwordx4 v[104:107], v[104:105], off offset:3072
	s_branch .LBB0_1438

	.amdhsa_kernel _Z10fwd_kernel4Args
		.amdhsa_group_segment_fixed_size 0
		.amdhsa_private_segment_fixed_size 0
		.amdhsa_kernarg_size 520
		.amdhsa_user_sgpr_count 2
		.amdhsa_user_sgpr_dispatch_ptr 0
		.amdhsa_user_sgpr_queue_ptr 0
		.amdhsa_user_sgpr_kernarg_segment_ptr 1
		.amdhsa_user_sgpr_dispatch_id 0
		.amdhsa_user_sgpr_kernarg_preload_length 0
		.amdhsa_user_sgpr_kernarg_preload_offset 0
		.amdhsa_user_sgpr_private_segment_size 0
		.amdhsa_uses_dynamic_stack 0
		.amdhsa_enable_private_segment 0
		.amdhsa_system_sgpr_workgroup_id_x 1
		.amdhsa_system_sgpr_workgroup_id_y 0
		.amdhsa_system_sgpr_workgroup_id_z 0
		.amdhsa_system_sgpr_workgroup_info 0
		.amdhsa_system_vgpr_workitem_id 0
		.amdhsa_next_free_vgpr 256
		.amdhsa_next_free_sgpr 102
		.amdhsa_accum_offset 256
		.amdhsa_reserve_vcc 1
		.amdhsa_float_round_mode_32 0
		.amdhsa_float_round_mode_16_64 0
		.amdhsa_float_denorm_mode_32 3
		.amdhsa_float_denorm_mode_16_64 3
		.amdhsa_dx10_clamp 1
		.amdhsa_ieee_mode 1
		.amdhsa_fp16_overflow 0
		.amdhsa_tg_split 0
		.amdhsa_exception_fp_ieee_invalid_op 0
		.amdhsa_exception_fp_denorm_src 0
		.amdhsa_exception_fp_ieee_div_zero 0
		.amdhsa_exception_fp_ieee_overflow 0
		.amdhsa_exception_fp_ieee_underflow 0
		.amdhsa_exception_fp_ieee_inexact 0
		.amdhsa_exception_int_div_zero 0
	.end_amdhsa_kernel

amdhsa.kernels:
  - .agpr_count:     0
    .args:
      - .offset:         0
        .size:           264
        .value_kind:     by_value
      - .offset:         264
        .size:           4
        .value_kind:     hidden_block_count_x
      - .offset:         268
        .size:           4
        .value_kind:     hidden_block_count_y
      - .offset:         272
        .size:           4
        .value_kind:     hidden_block_count_z
      - .offset:         276
        .size:           2
        .value_kind:     hidden_group_size_x
      - .offset:         278
        .size:           2
        .value_kind:     hidden_group_size_y
      - .offset:         280
        .size:           2
        .value_kind:     hidden_group_size_z
      - .offset:         282
        .size:           2
        .value_kind:     hidden_remainder_x
      - .offset:         284
        .size:           2
        .value_kind:     hidden_remainder_y
      - .offset:         286
        .size:           2
        .value_kind:     hidden_remainder_z
      - .offset:         304
        .size:           8
        .value_kind:     hidden_global_offset_x
      - .offset:         312
        .size:           8
        .value_kind:     hidden_global_offset_y
      - .offset:         320
        .size:           8
        .value_kind:     hidden_global_offset_z
      - .offset:         328
        .size:           2
        .value_kind:     hidden_grid_dims
      - .offset:         384
        .size:           4
        .value_kind:     hidden_dynamic_lds_size
    .group_segment_fixed_size: 0
    .kernarg_segment_align: 8
    .kernarg_segment_size: 520
    .language:       OpenCL C
    .language_version:
      - 2
      - 0
    .max_flat_workgroup_size: 512
    .name:           _Z10fwd_kernel4Args
    .private_segment_fixed_size: 0
    .sgpr_count:     108
    .sgpr_spill_count: 134
    .symbol:         _Z10fwd_kernel4Args.kd
    .uniform_work_group_size: 1
    .uses_dynamic_stack: false
    .vgpr_count:     256
    .vgpr_spill_count: 0
    .wavefront_size: 64
